# v3 + one static s_setprio 1 for waves 4-7 before the GQA tile loop (reset after it)
# speedup vs baseline: 1.0003x; 1.0003x over previous
.Lfa_entry:
	s_mov_b32 s29, 0
	s_mov_b32 s40, 1
	s_add_i32 s41, s23, 0xfffff000
	s_movk_i32 s10, 0x6a00
	v_add3_u32 v217, v201, v202, s10
	v_add_u32_e32 v216, v210, v208
	v_add_u32_e32 v218, v211, v200
	v_add_u32_e32 v208, 9216, v218
	v_add_u32_e32 v210, 13568, v218
	v_add_u32_e32 v200, 27136, v218
	v_add_u32_e32 v211, 31488, v218
	s_nop 7
	s_nop 7
	v_max3_f32 v214, v48, v64, v49
	v_max3_f32 v214, v214, v65, v50
	v_max3_f32 v214, v214, v66, v51
	v_max3_f32 v214, v214, v67, v52
	v_max3_f32 v214, v214, v68, v53
	v_max3_f32 v214, v214, v69, v54
	v_max3_f32 v214, v214, v70, v55
	v_max3_f32 v214, v214, v71, v56
	v_max3_f32 v214, v214, v72, v57
	v_max3_f32 v214, v214, v73, v58
	v_max3_f32 v214, v214, v74, v59
	v_max3_f32 v214, v214, v75, v60
	v_max3_f32 v214, v214, v76, v61
	v_max3_f32 v214, v214, v77, v62
	v_max3_f32 v214, v214, v78, v63
	v_max_f32_e32 v214, v214, v79
	v_mov_b32_e32 v218, v214
	s_nop 1
	v_permlane32_swap_b32_e32 v214, v218
	v_max_f32_e32 v214, v214, v218
	v_readlane_b32 s10, v252, 6
	s_cmp_lt_u32 s10, 0x100
	s_cbranch_scc1 .Lfa_noprio
	s_setprio 1
.Lfa_noprio:
.Lfa_loop:
	ds_read_b128 v[112:115], v216 offset:17920
	ds_read_b128 v[116:119], v216 offset:22528
	ds_read_b128 v[120:123], v216 offset:17952
	ds_read_b128 v[124:127], v216 offset:22560
	ds_read2_b64 v[128:131], v208 offset1:2
	ds_read2_b64 v[132:135], v210 offset1:2
	ds_read2_b64 v[136:139], v208 offset0:4 offset1:6
	ds_read2_b64 v[140:143], v210 offset0:4 offset1:6
	s_cmp_lg_u32 s40, 0
	s_cbranch_scc1 .Lfa_resc0
	v_cmp_lt_f32_e32 vcc, 0x40c00000, v214
	s_cbranch_vccnz .Lfa_resc0

.Lfa_cont3:
	v_exp_f32_e32 v80, v80
	v_exp_f32_e32 v81, v81
	v_exp_f32_e32 v82, v82
	v_exp_f32_e32 v83, v83
	s_waitcnt lgkmcnt(7)
	v_mfma_f32_32x32x16_bf16 v[48:63], v[112:115], v[144:147], v[32:47]
	v_exp_f32_e32 v84, v84
	v_exp_f32_e32 v85, v85
	v_exp_f32_e32 v86, v86
	v_exp_f32_e32 v87, v87
	s_waitcnt lgkmcnt(6)
	v_mfma_f32_32x32x16_bf16 v[64:79], v[116:119], v[144:147], v[32:47]
	v_add_f32_e32 v213, v80, v81
	v_add_f32_e32 v213, v213, v82
	v_add_f32_e32 v213, v213, v83
	s_waitcnt lgkmcnt(5)
	v_mfma_f32_32x32x16_bf16 v[48:63], v[120:123], v[148:151], v[48:63]
	v_add_f32_e32 v213, v213, v84
	v_add_f32_e32 v213, v213, v85
	v_add_f32_e32 v213, v213, v86
	v_add_f32_e32 v213, v213, v87
	s_waitcnt lgkmcnt(4)
	v_mfma_f32_32x32x16_bf16 v[64:79], v[124:127], v[148:151], v[64:79]
	v_cvt_pk_bf16_f32 v80, v80, v81
	v_cvt_pk_bf16_f32 v81, v82, v83
	v_cvt_pk_bf16_f32 v82, v84, v85
	v_cvt_pk_bf16_f32 v83, v86, v87
	ds_read_b128 v[112:115], v216 offset:64
	ds_read_b128 v[116:119], v216 offset:4672
	ds_read_b128 v[120:123], v216 offset:96
	ds_read_b128 v[124:127], v216 offset:4704
	v_exp_f32_e32 v88, v88
	v_exp_f32_e32 v89, v89
	s_waitcnt lgkmcnt(7)
	v_mfma_f32_32x32x16_bf16 v[0:15], v[128:131], v[80:83], v[0:15]
	v_exp_f32_e32 v90, v90
	v_exp_f32_e32 v91, v91
	v_exp_f32_e32 v92, v92
	s_waitcnt lgkmcnt(6)
	v_mfma_f32_32x32x16_bf16 v[16:31], v[132:135], v[80:83], v[16:31]
	v_exp_f32_e32 v93, v93
	v_exp_f32_e32 v94, v94
	v_exp_f32_e32 v95, v95
	s_waitcnt lgkmcnt(3)
	v_mfma_f32_32x32x16_bf16 v[48:63], v[112:115], v[152:155], v[48:63]
	v_add_f32_e32 v213, v213, v88
	v_add_f32_e32 v213, v213, v89
	v_add_f32_e32 v213, v213, v90
	v_add_f32_e32 v213, v213, v91
	s_waitcnt lgkmcnt(2)
	v_mfma_f32_32x32x16_bf16 v[64:79], v[116:119], v[152:155], v[64:79]
	v_add_f32_e32 v213, v213, v92
	v_add_f32_e32 v213, v213, v93
	v_add_f32_e32 v213, v213, v94
	v_add_f32_e32 v213, v213, v95
	v_cvt_pk_bf16_f32 v88, v88, v89
	v_cvt_pk_bf16_f32 v89, v90, v91
	v_cvt_pk_bf16_f32 v90, v92, v93
	v_cvt_pk_bf16_f32 v91, v94, v95
	v_exp_f32_e32 v96, v96
	v_exp_f32_e32 v97, v97
	v_mfma_f32_32x32x16_bf16 v[0:15], v[136:139], v[88:91], v[0:15]
	v_exp_f32_e32 v98, v98
	v_exp_f32_e32 v99, v99
	v_exp_f32_e32 v100, v100
	v_mfma_f32_32x32x16_bf16 v[16:31], v[140:143], v[88:91], v[16:31]
	ds_read2_b64 v[128:131], v200 offset0:8 offset1:10
	ds_read2_b64 v[132:135], v211 offset0:8 offset1:10
	ds_read2_b64 v[136:139], v200 offset0:12 offset1:14
	ds_read2_b64 v[140:143], v211 offset0:12 offset1:14
	v_exp_f32_e32 v101, v101
	v_exp_f32_e32 v102, v102
	v_exp_f32_e32 v103, v103
	s_waitcnt lgkmcnt(5)
	v_mfma_f32_32x32x16_bf16 v[48:63], v[120:123], v[156:159], v[48:63]
	v_add_f32_e32 v213, v213, v96
	v_add_f32_e32 v213, v213, v97
	v_add_f32_e32 v213, v213, v98
	v_add_f32_e32 v213, v213, v99
	s_waitcnt lgkmcnt(4)
	v_mfma_f32_32x32x16_bf16 v[64:79], v[124:127], v[156:159], v[64:79]
	v_add_f32_e32 v213, v213, v100
	v_add_f32_e32 v213, v213, v101
	v_add_f32_e32 v213, v213, v102
	v_add_f32_e32 v213, v213, v103
	v_cvt_pk_bf16_f32 v96, v96, v97
	v_cvt_pk_bf16_f32 v97, v98, v99
	v_cvt_pk_bf16_f32 v98, v100, v101
	v_cvt_pk_bf16_f32 v99, v102, v103
	v_exp_f32_e32 v104, v104
	v_exp_f32_e32 v105, v105
	s_waitcnt lgkmcnt(3)
	v_mfma_f32_32x32x16_bf16 v[0:15], v[128:131], v[96:99], v[0:15]
	v_exp_f32_e32 v106, v106
	v_exp_f32_e32 v107, v107
	v_exp_f32_e32 v108, v108
	s_waitcnt lgkmcnt(2)
	v_mfma_f32_32x32x16_bf16 v[16:31], v[132:135], v[96:99], v[16:31]
	v_exp_f32_e32 v109, v109
	v_exp_f32_e32 v110, v110
	v_exp_f32_e32 v111, v111
	s_add_i32 s10, s29, 9
	s_min_i32 s10, s10, 0x43
	s_cmp_lt_i32 s10, 64
	s_cselect_b32 s11, s20, s41
	s_lshl_b32 s10, s10, 6
	s_add_i32 s10, s10, s11
	v_add_u32_e32 v112, s10, v197
	s_movk_i32 s10, 0x4a00
	v_mad_i64_i32 v[112:113], s[10:11], v112, s10, v[204:205]
	s_add_i32 s14, s29, 8
	s_min_i32 s14, s14, 0x43
	s_lshl_b32 s14, s14, 6
	s_mov_b32 s15, 0
	v_add_f32_e32 v213, v213, v104
	v_add_f32_e32 v213, v213, v105
	v_add_f32_e32 v213, v213, v106
	v_add_f32_e32 v213, v213, v107
	s_waitcnt vmcnt(7)
	ds_write_b128 v199, v[184:187] offset:17920
	s_waitcnt vmcnt(6)
	ds_write2_b64 v203, v[188:189], v[190:191] offset1:1
	v_lshl_add_u64 v[114:115], s[14:15], 1, v[206:207]
	global_load_dwordx4 v[184:187], v[112:113], off
	global_load_dwordx4 v[188:191], v[114:115], off
	v_add_f32_e32 v213, v213, v108
	v_add_f32_e32 v213, v213, v109
	v_add_f32_e32 v213, v213, v110
	v_add_f32_e32 v213, v213, v111
	v_cvt_pk_bf16_f32 v104, v104, v105
	v_cvt_pk_bf16_f32 v105, v106, v107
	v_cvt_pk_bf16_f32 v106, v108, v109
	v_cvt_pk_bf16_f32 v107, v110, v111
	v_max3_f32 v214, v48, v64, v49
	v_max3_f32 v214, v214, v65, v50
	v_max3_f32 v214, v214, v66, v51
	v_max3_f32 v214, v214, v67, v52
	v_max3_f32 v214, v214, v68, v53
	v_max3_f32 v214, v214, v69, v54
	v_max3_f32 v214, v214, v70, v55
	v_max3_f32 v214, v214, v71, v56
	v_add_f32_e32 v212, v212, v213
	s_waitcnt lgkmcnt(3)
	v_mfma_f32_32x32x16_bf16 v[0:15], v[136:139], v[104:107], v[0:15]
	v_max3_f32 v214, v214, v72, v57
	v_max3_f32 v214, v214, v73, v58
	v_max3_f32 v214, v214, v74, v59
	v_max3_f32 v214, v214, v75, v60
	s_waitcnt lgkmcnt(2)
	v_mfma_f32_32x32x16_bf16 v[16:31], v[140:143], v[104:107], v[16:31]
	v_max3_f32 v214, v214, v76, v61
	v_max3_f32 v214, v214, v77, v62
	v_max3_f32 v214, v214, v78, v63
	v_max_f32_e32 v214, v214, v79
	v_mov_b32_e32 v218, v214
	s_nop 1
	v_permlane32_swap_b32_e32 v214, v218
	v_max_f32_e32 v214, v214, v218
	s_waitcnt lgkmcnt(0)
	s_barrier
	s_add_i32 s29, s29, 4
	s_cmp_lt_i32 s29, 68
	s_cbranch_scc1 .Lfa_loop
	s_setprio 0
	s_branch .LBB0_908
